# g2p + static priority raise on waves 0-3 (instead of 4-7) through phases 2-4, MLA raise unchanged (per-half A/B for the GLA/dilated phases)
# baseline (speedup 1.0000x reference)
; #define INP(k) ldptr(PTAB, (k))
; __global__ void __launch_bounds__(NWAVES * 64, 2) fwd_kernel(Args args) {
;     ...
;             { BODY_LOCALS
;               for (int it = vcu; it < 1024; it += G) { float wa[16], ba; gla_alpha_load(wa, ba, INP(6) + (size_t)l * 16 * 512, INP(7) + l * 512, (it >> 6) & 3, tid);
;                   const GlaPre cur = gla_blr_load(WSP(WS_ZABC), (size_t)(it >> 8) * SEQ + 64 * (it & 63), tid);
;                   gla_g1(ring, WSP(WS_ZABC), ((bf16*)xo), (float*)(ws + WS_GLADEC), cur, wa, ba, it, tid); } }
.LBB0_913:
	s_or_b64 exec, exec, s[38:39]
	s_lshl_b32 s0, s88, 9
	s_mov_b32 s1, s95
	v_writelane_b32 v255, s0, 31
	v_readlane_b32 s12, v252, 6
	v_readlane_b32 s8, v252, 4
	v_writelane_b32 v255, s1, 32
	v_readlane_b32 s18, v252, 12
	v_readlane_b32 s19, v252, 13
	v_readlane_b32 s0, v252, 32
	v_readlane_b32 s9, v252, 5
	s_mov_b64 s[4:5], s[18:19]
	v_readlane_b32 s1, v252, 33
	s_waitcnt lgkmcnt(0)
	s_barrier
	s_lshl_b32 s50, s88, 13
	s_mov_b32 s51, s95
	v_mbcnt_lo_u32_b32 v0, -1, 0
	v_mbcnt_hi_u32_b32 v0, -1, v0
	s_andn2_b64 vcc, exec, s[0:1]
	v_readlane_b32 s13, v252, 7
	v_readlane_b32 s14, v252, 8
	v_readlane_b32 s15, v252, 9
	v_readlane_b32 s16, v252, 10
	v_readlane_b32 s17, v252, 11
	v_mbcnt_lo_u32_b32 v0, -1, 0
	v_mbcnt_hi_u32_b32 v0, -1, v0
	s_cbranch_vccnz .LBB0_924
	v_readlane_b32 s0, v252, 37
	s_add_u32 s6, s8, 0x15600000
	s_addc_u32 s7, s9, 0
	v_add_u32_e32 v72, s0, v0
	v_readlane_b32 s0, v254, 14
	v_ashrrev_i32_e32 v66, 4, v72
	v_and_b32_e32 v0, 15, v0
	s_add_u32 s10, s8, s0
	v_readlane_b32 s0, v254, 15
	v_readlane_b32 s12, v254, 8
	v_readlane_b32 s14, v254, 12
	v_and_b32_e32 v73, 0x7f, v72
	v_ashrrev_i32_e32 v67, 31, v66
	s_addc_u32 s11, s9, s0
	v_lshlrev_b32_e32 v68, 1, v0
	v_readlane_b32 s13, v254, 9
	v_readlane_b32 s0, v253, 58
	s_mov_b32 s1, s14
	v_readlane_b32 s15, v254, 13
	v_readlane_b32 s98, v252, 37
	s_nop 3
	s_cmpk_lt_u32 s98, 0x100
	s_cbranch_scc0 .Lprio_g1_done
	s_setprio 1

; #define INP(k) ldptr(PTAB, (k))
; __global__ void __launch_bounds__(NWAVES * 64, 2) fwd_kernel(Args args) {
;     ...
;             { BODY_LOCALS
;               for (int it = vcu; it < 1024; it += G) { float wa[16], ba; gla_alpha_load(wa, ba, INP(6) + (size_t)l * 16 * 512, INP(7) + l * 512, (it >> 6) & 3, tid);
;                   const GlaPre cur = gla_blr_load(WSP(WS_ZABC), (size_t)(it >> 8) * SEQ + 64 * (it & 63), tid);
;                   gla_g3(ring, WSP(WS_ZABC), ((bf16*)xo), WSP(WS_OABC), cur, wa, ba, INP(8) + l * 1024, it, tid); } }
.LBB0_1110:
	s_or_b64 exec, exec, s[38:39]
	v_readlane_b32 s8, v252, 6
	v_readlane_b32 s4, v252, 4
	v_readlane_b32 s14, v252, 12
	v_readlane_b32 s15, v252, 13
	v_readlane_b32 s0, v252, 32
	v_readlane_b32 s5, v252, 5
	s_mov_b64 s[6:7], s[14:15]
	v_readlane_b32 s1, v252, 33
	s_waitcnt lgkmcnt(0)
	s_barrier
	v_mbcnt_lo_u32_b32 v0, -1, 0
	v_mbcnt_hi_u32_b32 v0, -1, v0
	s_and_b64 vcc, exec, s[0:1]
	v_readlane_b32 s9, v252, 7
	v_readlane_b32 s10, v252, 8
	v_readlane_b32 s11, v252, 9
	v_readlane_b32 s12, v252, 10
	v_readlane_b32 s13, v252, 11
	v_mbcnt_lo_u32_b32 v0, -1, 0
	v_mbcnt_hi_u32_b32 v0, -1, v0
	s_cbranch_vccz .LBB0_1119
	v_readlane_b32 s0, v255, 23
	s_lshl_b32 s94, s0, 10
	s_add_u32 s8, s4, 0x15600000
	v_readlane_b32 s0, v252, 37
	s_addc_u32 s9, s5, 0
	v_readlane_b32 s1, v255, 24
	v_add_u32_e32 v136, s0, v0
	s_add_u32 s0, s4, 0x29e00000
	v_ashrrev_i32_e32 v130, 4, v136
	v_and_b32_e32 v0, 15, v0
	s_addc_u32 s1, s5, 0
	v_readlane_b32 s12, v254, 8
	v_readlane_b32 s4, v254, 12
	v_and_b32_e32 v137, 0x7f, v136
	v_ashrrev_i32_e32 v131, 31, v130
	v_lshlrev_b32_e32 v132, 1, v0
	s_lshl_b64 s[10:11], s[94:95], 2
	v_readlane_b32 s13, v254, 9
	v_readlane_b32 s16, v253, 58
	s_mov_b32 s17, s4
	v_readlane_b32 s5, v254, 13
	v_readlane_b32 s98, v252, 37
	s_nop 3
	s_cmpk_lt_u32 s98, 0x100
	s_cbranch_scc0 .Lprio_g3_done
	s_setprio 1

; #define PHASE_LOCALS unsigned long long wsu_ = (unsigned long long)ws0; asm volatile("" : "+s"(wsu_)); unsigned char* ws = (unsigned char*)(GAS unsigned char*)wsu_; unsigned long long xou_ = (unsigned long long)xo0; asm volatile("" : "+s"(xou_)); float* xo = (float*)(GAS float*)xou_; BODY_LOCALS
; __global__ void __launch_bounds__(NWAVES * 64, 2) fwd_kernel(Args args) {
;     ...
;         if (((PHASE_MASK >> 5) & 1) && IN(P + 5)) for (int rep_ = 0; rep_ < 1 + ((PHASE_TWICE >> 5) & 1); ++rep_) { PHASE_LOCALS
;             { BODY_LOCALS mla_attn_phase(ring, WSP(WS_MLAQ), MLAKV_D, WSP(WS_ZABC), WSP(WS_OABC), ((float*)(ws + WS_ROPE)), ((float*)(ws + WS_ROPE) + SEQ * 32), vcu, G, tid); }
.LBB0_1119:
	v_readlane_b32 s12, v252, 6
	v_readlane_b32 s8, v252, 4
	v_readlane_b32 s18, v252, 12
	v_readlane_b32 s19, v252, 13
	v_readlane_b32 s9, v252, 5
	s_mov_b64 s[6:7], s[18:19]
	v_mbcnt_lo_u32_b32 v0, -1, 0
	v_mbcnt_hi_u32_b32 v0, -1, v0
	v_readlane_b32 s0, v252, 37
	s_nop 3
	s_setprio 0
	s_cmpk_lt_u32 s0, 0x100
	s_cbranch_scc1 .Lmla_prio_done
	s_setprio 1
